# cmp pass 1: exps read the score MFMA outputs directly (32 phi-copy v_mov per item gone), rescale adds its offset in place, one v_max instead of three canonicalising ones
# speedup vs baseline: 1.0126x; 1.0106x over previous
; __device__ __forceinline__ float xmax16(float v) { float a = v, b = v; PL_SWAP16(a, b); return fmaxf(a, b); }
; __device__ __forceinline__ float xmax32(float v) { float a = v, b = v; PL_SWAP32(a, b); return fmaxf(a, b); }
; template <bool WITH_O, class G> __device__ __forceinline__ void online_smc(f32x4 (&s)[4], G& g, const float ref) {
;     float mx = s[0][0];
; #pragma unroll
;     for (int T_ = 0; T_ < 4; ++T_)
; #pragma unroll
;         for (int i = 0; i < 4; ++i) mx = fmaxf(mx, s[T_][i]);
;     const float t = mx + ref;
;     if (!__all(t <= g.m + SM_THR)) {
;         const float mr = xmax32(xmax16(t));
;         const float mn = fmaxf(g.m, mr); const float al = __builtin_amdgcn_exp2f(g.m - mn); g.m = mn; g.l *= al;
;         if (WITH_O) {
; #pragma unroll
;             for (int dt = 0; dt < 8; ++dt) g.o[dt] = g.o[dt] * al; }
;         const float d = ref - mn;
; #pragma unroll
;         for (int T_ = 0; T_ < 4; ++T_)
; #pragma unroll
;             for (int i = 0; i < 4; ++i) s[T_][i] += d;
;     }
;     float ps = 0.f;
; #pragma unroll
;     for (int T_ = 0; T_ < 4; ++T_)
; #pragma unroll
;         for (int i = 0; i < 4; ++i) { s[T_][i] = __builtin_amdgcn_exp2f(s[T_][i]); ps += s[T_][i]; }
;     g.l += ps;
.LBB0_1579:
	s_mov_b64 s[22:23], -1
	s_and_b64 vcc, exec, s[56:57]
	s_cbranch_vccz .LBB0_1585
	v_max_f32_e32 v134, v108, v109
	v_max3_f32 v134, v134, v110, v111
	v_max3_f32 v134, v134, v104, v105
	v_max3_f32 v134, v134, v106, v107
	v_max3_f32 v134, v134, v100, v101
	v_max3_f32 v134, v134, v102, v103
	v_max3_f32 v134, v134, v96, v97
	v_max3_f32 v134, v134, v98, v99
	v_pk_add_f32 v[158:159], v[140:141], v[134:135]
	v_mov_b32_e32 v194, v141
	v_cmp_le_f32_e32 vcc, v158, v159
	s_cmp_eq_u64 vcc, exec
	v_mov_b32_e32 v195, v191
	s_cbranch_scc1 .LBB0_1582
	v_mov_b32_e32 v134, v158
	s_nop 1
	v_permlane16_swap_b32 v158, v134
	v_max_f32_e32 v134, v134, v134
	v_max_f32_e32 v144, v158, v158
	v_max_f32_e32 v134, v144, v134
	v_mov_b32_e32 v144, v134
	s_nop 1
	v_permlane32_swap_b32 v134, v144
	v_max3_f32 v194, v141, v134, v144
	v_sub_f32_e32 v134, v141, v194
	v_exp_f32_e32 v134, v134
	v_sub_f32_e32 v144, v140, v194
	v_mul_f32_e32 v195, v191, v134
	v_add_f32_e32 v96, v96, v144
	v_add_f32_e32 v97, v97, v144
	v_add_f32_e32 v98, v98, v144
	v_add_f32_e32 v99, v99, v144
	v_add_f32_e32 v100, v100, v144
	v_add_f32_e32 v101, v101, v144
	v_add_f32_e32 v102, v102, v144
	v_add_f32_e32 v103, v103, v144
	v_add_f32_e32 v104, v104, v144
	v_add_f32_e32 v105, v105, v144
	v_add_f32_e32 v106, v106, v144
	v_add_f32_e32 v107, v107, v144
	v_add_f32_e32 v108, v108, v144
	v_add_f32_e32 v109, v109, v144
	v_add_f32_e32 v110, v110, v144
	v_add_f32_e32 v111, v111, v144
.LBB0_1582:
	v_max_f32_e32 v134, v88, v89
	v_max3_f32 v134, v134, v90, v91
	v_max3_f32 v134, v134, v84, v85
	v_max3_f32 v134, v134, v86, v87
	v_max3_f32 v134, v134, v80, v81
	v_max3_f32 v134, v134, v82, v83
	v_max3_f32 v134, v134, v92, v93
	v_max3_f32 v134, v134, v94, v95
	v_pk_add_f32 v[170:171], v[138:139], v[134:135]
	v_mov_b32_e32 v140, v190
	v_cmp_le_f32_e32 vcc, v170, v171
	s_cmp_eq_u64 vcc, exec
	v_mov_b32_e32 v134, v139
	s_cbranch_scc1 .LBB0_1584
	v_mov_b32_e32 v134, v170
	s_nop 1
	v_permlane16_swap_b32 v170, v134
	v_max_f32_e32 v134, v134, v134
	v_max_f32_e32 v140, v170, v170
	v_max_f32_e32 v134, v140, v134
	v_mov_b32_e32 v140, v134
	s_nop 1
	v_permlane32_swap_b32 v134, v140
	v_max3_f32 v134, v139, v134, v140
	v_sub_f32_e32 v140, v139, v134
	v_exp_f32_e32 v140, v140
	v_sub_f32_e32 v138, v138, v134
	v_mul_f32_e32 v140, v190, v140
	v_add_f32_e32 v80, v80, v138
	v_add_f32_e32 v81, v81, v138
	v_add_f32_e32 v82, v82, v138
	v_add_f32_e32 v83, v83, v138
	v_add_f32_e32 v84, v84, v138
	v_add_f32_e32 v85, v85, v138
	v_add_f32_e32 v86, v86, v138
	v_add_f32_e32 v87, v87, v138
	v_add_f32_e32 v88, v88, v138
	v_add_f32_e32 v89, v89, v138
	v_add_f32_e32 v90, v90, v138
	v_add_f32_e32 v91, v91, v138
	v_add_f32_e32 v92, v92, v138
	v_add_f32_e32 v93, v93, v138
	v_add_f32_e32 v94, v94, v138
	v_add_f32_e32 v95, v95, v138
.LBB0_1584:
	v_exp_f32_e32 v138, v108
	v_exp_f32_e32 v150, v109
	v_exp_f32_e32 v151, v110
	v_exp_f32_e32 v156, v111
	v_add_f32_e32 v138, 0, v138
	v_add_f32_e32 v138, v138, v150
	v_exp_f32_e32 v150, v104
	v_add_f32_e32 v138, v151, v138
	v_exp_f32_e32 v151, v105
	v_exp_f32_e32 v152, v106
	v_add_f32_e32 v138, v156, v138
	v_exp_f32_e32 v153, v107
	v_add_f32_e32 v138, v150, v138
	v_exp_f32_e32 v150, v100
	v_add_f32_e32 v138, v151, v138
	v_exp_f32_e32 v148, v101
	v_add_f32_e32 v138, v152, v138
	v_exp_f32_e32 v149, v102
	v_add_f32_e32 v138, v153, v138
	v_exp_f32_e32 v151, v103
	v_add_f32_e32 v138, v150, v138
	v_exp_f32_e32 v144, v96
	v_add_f32_e32 v138, v148, v138
	v_exp_f32_e32 v145, v97
	v_add_f32_e32 v138, v149, v138
	v_exp_f32_e32 v146, v98
	v_add_f32_e32 v138, v151, v138
	v_exp_f32_e32 v147, v99
	v_add_f32_e32 v138, v144, v138
	v_add_f32_e32 v138, v145, v138
	v_add_f32_e32 v138, v146, v138
	v_add_f32_e32 v138, v147, v138
	v_add_f32_e32 v144, v195, v138
	v_exp_f32_e32 v138, v88
	v_exp_f32_e32 v145, v89
	v_exp_f32_e32 v146, v90
	v_exp_f32_e32 v147, v91
	v_add_f32_e32 v138, 0, v138
	v_add_f32_e32 v138, v138, v145
	v_exp_f32_e32 v145, v84
	v_add_f32_e32 v138, v146, v138
	v_exp_f32_e32 v146, v85
	v_add_f32_e32 v138, v147, v138
	v_exp_f32_e32 v147, v86
	v_exp_f32_e32 v148, v87
	v_add_f32_e32 v138, v145, v138
	v_exp_f32_e32 v145, v80
	v_add_f32_e32 v138, v146, v138
	v_exp_f32_e32 v146, v81
	v_add_f32_e32 v138, v147, v138
	v_exp_f32_e32 v147, v82
	v_add_f32_e32 v138, v148, v138
	v_exp_f32_e32 v148, v83
	v_add_f32_e32 v138, v145, v138
	v_exp_f32_e32 v145, v92
	v_add_f32_e32 v138, v146, v138
	v_exp_f32_e32 v146, v93
	v_add_f32_e32 v138, v147, v138
	v_exp_f32_e32 v147, v94
	v_add_f32_e32 v138, v148, v138
	v_exp_f32_e32 v148, v95
	v_add_f32_e32 v138, v145, v138
	v_add_f32_e32 v138, v146, v138
	v_add_f32_e32 v138, v147, v138
	v_add_f32_e32 v138, v148, v138
	v_add_f32_e32 v145, v140, v138
	s_branch .LBB0_1570
